# grid barrier rewritten: per-XCD arrival counter, leader raises a per-XCD flag, every workgroup polls the 16 flags with one load (two hops fewer); first barrier unchanged
# speedup vs baseline: 1.0018x; 1.0018x over previous
; __device__ __forceinline__ unsigned xb_ld(unsigned* p)              { return __hip_atomic_load(p, __ATOMIC_RELAXED, __HIP_MEMORY_SCOPE_AGENT); }
; __device__ __forceinline__ unsigned xb_add(unsigned* p, unsigned v) { return __hip_atomic_fetch_add(p, v, __ATOMIC_RELAXED, __HIP_MEMORY_SCOPE_AGENT); }
; #define XB_SPIN(cond, bar) do { unsigned _sp = 0; while (cond) { __builtin_amdgcn_s_sleep(1); \
;     if ((++_sp & 255u) == 0u) { if (xb_ld(&(bar)[XB_TMO])) break; if (_sp > XB_SPIN_CAP) { atomicAdd(&(bar)[XB_TMO], 1u); break; } } } } while (0)
; __device__ __forceinline__ void xcd_barrier(const XcdBarrier& b) {
;     asm volatile("s_waitcnt vmcnt(0)" ::: "memory");
;     __syncthreads();
;     if (threadIdx.x == 0) {
;         unsigned* bar = b.bar;
;         __builtin_amdgcn_s_waitcnt(0);
;         unsigned nloc = b.st[0], nx = b.st[1];
;         if (nloc == 0u) { xcd_barrier_complete(bar, b.x, nloc, nx); b.st[0] = nloc; b.st[1] = nx; }
;         const unsigned old = xb_add(&bar[XB_XSUB(b.x)], 1u);
;         const unsigned gen = old / nloc;
;         if (old + 1u == (gen + 1u) * nloc) {
;             __builtin_amdgcn_fence(__ATOMIC_RELEASE, "agent");
;             asm volatile("s_waitcnt vmcnt(0)" ::: "memory");
;             const unsigned og = xb_add(&bar[XB_TOP], 1u);
;             const unsigned tg = og / nx;
;             if (og + 1u == (tg + 1u) * nx) xb_add(&bar[XB_TOPGEN], 1u);
;             else XB_SPIN(xb_ld(&bar[XB_TOPGEN]) == tg, bar);
;             __builtin_amdgcn_fence(__ATOMIC_ACQUIRE, "agent");
;             xb_add(&bar[XB_XGEN(b.x)], 1u);
;             asm volatile("s_waitcnt vmcnt(0)" ::: "memory");
;         } else {
;             XB_SPIN(xb_ld(&bar[XB_XGEN(b.x)]) == gen, bar);
;             __builtin_amdgcn_fence(__ATOMIC_ACQUIRE, "agent");
;             asm volatile("s_waitcnt vmcnt(0)" ::: "memory");
;         }
;     }
;     __syncthreads();
.LBB0_93:
	s_cmp_lt_i32 s95, 3
	s_cbranch_scc1 .LBB0_143
	s_waitcnt vmcnt(0)
	v_cmp_eq_u32_e32 vcc, 0, v0
	s_waitcnt lgkmcnt(0)
	s_barrier
	s_and_saveexec_b64 s[0:1], vcc
	s_cbranch_execz .LBB0_142
	v_readlane_b32 s4, v246, 22
	v_readlane_b32 s5, v246, 21
	s_waitcnt vmcnt(0) expcnt(0) lgkmcnt(0)
	s_nop 1
	v_mov_b32_e32 v1, s4
	ds_read_b32 v2, v1
	ds_read_b32 v3, v1 offset:4
	ds_read_b32 v4, v1 offset:8
	s_lshl_b32 s5, s5, 6
	s_add_u32 s6, s92, 0xf800
	s_addc_u32 s7, s93, 0
	s_add_u32 s8, s92, 0xfc00
	s_addc_u32 s9, s93, 0
	v_mov_b32_e32 v5, s5
	v_mov_b32_e32 v6, 1
	global_atomic_add v6, v5, v6, s[6:7] sc0
	s_waitcnt lgkmcnt(0)
	v_add_u32_e32 v4, 1, v4
	ds_write_b32 v1, v4 offset:8
	v_mul_lo_u32 v7, v4, v2
	s_waitcnt vmcnt(0)
	v_add_u32_e32 v6, 1, v6
	v_cmp_eq_u32_e32 vcc, v6, v7
	s_and_b64 vcc, exec, vcc
	s_cbranch_vccz .Lgb0_poll
	buffer_wbl2 sc1
	s_waitcnt vmcnt(0)
	s_lshr_b32 s5, s5, 4
	v_mov_b32_e32 v5, s5
	global_atomic_umax v5, v4, s[8:9]
.Lgb0_poll:
	v_readfirstlane_b32 s10, v4
	v_readfirstlane_b32 s11, v3
	s_mov_b64 exec, 0xffff
	v_lshlrev_b32_e32 v5, 2, v0
	s_mov_b32 s12, 0
.Lgb0_loop:
	global_load_dword v6, v5, s[8:9] sc1
	s_waitcnt vmcnt(0)
	v_cmp_le_u32_e32 vcc, s10, v6
	s_bcnt1_i32_b64 s13, vcc
	s_cmp_ge_u32 s13, s11
	s_cbranch_scc1 .Lgb0_done
	s_sleep 1
	s_add_u32 s12, s12, 1
	s_cmp_lt_u32 s12, 0x40000
	s_cbranch_scc1 .Lgb0_loop
.Lgb0_done:
	buffer_inv sc1
	s_waitcnt vmcnt(0) lgkmcnt(0)

; __device__ __forceinline__ unsigned xb_ld(unsigned* p)              { return __hip_atomic_load(p, __ATOMIC_RELAXED, __HIP_MEMORY_SCOPE_AGENT); }
; __device__ __forceinline__ unsigned xb_add(unsigned* p, unsigned v) { return __hip_atomic_fetch_add(p, v, __ATOMIC_RELAXED, __HIP_MEMORY_SCOPE_AGENT); }
; #define XB_SPIN(cond, bar) do { unsigned _sp = 0; while (cond) { __builtin_amdgcn_s_sleep(1); \
;     if ((++_sp & 255u) == 0u) { if (xb_ld(&(bar)[XB_TMO])) break; if (_sp > XB_SPIN_CAP) { atomicAdd(&(bar)[XB_TMO], 1u); break; } } } } while (0)
; __device__ __forceinline__ void xcd_barrier(const XcdBarrier& b) {
;     asm volatile("s_waitcnt vmcnt(0)" ::: "memory");
;     __syncthreads();
;     if (threadIdx.x == 0) {
;         unsigned* bar = b.bar;
;         __builtin_amdgcn_s_waitcnt(0);
;         unsigned nloc = b.st[0], nx = b.st[1];
;         if (nloc == 0u) { xcd_barrier_complete(bar, b.x, nloc, nx); b.st[0] = nloc; b.st[1] = nx; }
;         const unsigned old = xb_add(&bar[XB_XSUB(b.x)], 1u);
;         const unsigned gen = old / nloc;
;         if (old + 1u == (gen + 1u) * nloc) {
;             __builtin_amdgcn_fence(__ATOMIC_RELEASE, "agent");
;             asm volatile("s_waitcnt vmcnt(0)" ::: "memory");
;             const unsigned og = xb_add(&bar[XB_TOP], 1u);
;             const unsigned tg = og / nx;
;             if (og + 1u == (tg + 1u) * nx) xb_add(&bar[XB_TOPGEN], 1u);
;             else XB_SPIN(xb_ld(&bar[XB_TOPGEN]) == tg, bar);
;             __builtin_amdgcn_fence(__ATOMIC_ACQUIRE, "agent");
;             xb_add(&bar[XB_XGEN(b.x)], 1u);
;             asm volatile("s_waitcnt vmcnt(0)" ::: "memory");
;         } else {
;             XB_SPIN(xb_ld(&bar[XB_XGEN(b.x)]) == gen, bar);
;             __builtin_amdgcn_fence(__ATOMIC_ACQUIRE, "agent");
;             asm volatile("s_waitcnt vmcnt(0)" ::: "memory");
;         }
;     }
;     __syncthreads();
.Lp3_after_pool:
	s_cmp_lt_i32 s95, 5
	s_cbranch_scc1 .LBB0_764
	s_waitcnt vmcnt(0)
	v_cmp_eq_u32_e32 vcc, 0, v0
	s_waitcnt vmcnt(0)
	s_barrier
	s_and_saveexec_b64 s[0:1], vcc
	s_cbranch_execz .LBB0_763
	v_readlane_b32 s4, v246, 22
	v_readlane_b32 s5, v246, 21
	s_waitcnt vmcnt(0) expcnt(0) lgkmcnt(0)
	s_nop 1
	v_mov_b32_e32 v1, s4
	ds_read_b32 v2, v1
	ds_read_b32 v3, v1 offset:4
	ds_read_b32 v4, v1 offset:8
	s_lshl_b32 s5, s5, 6
	s_add_u32 s6, s92, 0xf800
	s_addc_u32 s7, s93, 0
	s_add_u32 s8, s92, 0xfc00
	s_addc_u32 s9, s93, 0
	v_mov_b32_e32 v5, s5
	v_mov_b32_e32 v6, 1
	global_atomic_add v6, v5, v6, s[6:7] sc0
	s_waitcnt lgkmcnt(0)
	v_add_u32_e32 v4, 1, v4
	ds_write_b32 v1, v4 offset:8
	v_mul_lo_u32 v7, v4, v2
	s_waitcnt vmcnt(0)
	v_add_u32_e32 v6, 1, v6
	v_cmp_eq_u32_e32 vcc, v6, v7
	s_and_b64 vcc, exec, vcc
	s_cbranch_vccz .Lgb1_poll
	buffer_wbl2 sc1
	s_waitcnt vmcnt(0)
	s_lshr_b32 s5, s5, 4
	v_mov_b32_e32 v5, s5
	global_atomic_umax v5, v4, s[8:9]

; __device__ __forceinline__ unsigned xb_ld(unsigned* p)              { return __hip_atomic_load(p, __ATOMIC_RELAXED, __HIP_MEMORY_SCOPE_AGENT); }
; __device__ __forceinline__ unsigned xb_add(unsigned* p, unsigned v) { return __hip_atomic_fetch_add(p, v, __ATOMIC_RELAXED, __HIP_MEMORY_SCOPE_AGENT); }
; #define XB_SPIN(cond, bar) do { unsigned _sp = 0; while (cond) { __builtin_amdgcn_s_sleep(1); \
;     if ((++_sp & 255u) == 0u) { if (xb_ld(&(bar)[XB_TMO])) break; if (_sp > XB_SPIN_CAP) { atomicAdd(&(bar)[XB_TMO], 1u); break; } } } } while (0)
; __device__ __forceinline__ void xcd_barrier(const XcdBarrier& b) {
;     asm volatile("s_waitcnt vmcnt(0)" ::: "memory");
;     __syncthreads();
;     if (threadIdx.x == 0) {
;         unsigned* bar = b.bar;
;         __builtin_amdgcn_s_waitcnt(0);
;         unsigned nloc = b.st[0], nx = b.st[1];
;         if (nloc == 0u) { xcd_barrier_complete(bar, b.x, nloc, nx); b.st[0] = nloc; b.st[1] = nx; }
;         const unsigned old = xb_add(&bar[XB_XSUB(b.x)], 1u);
;         const unsigned gen = old / nloc;
;         if (old + 1u == (gen + 1u) * nloc) {
;             __builtin_amdgcn_fence(__ATOMIC_RELEASE, "agent");
;             asm volatile("s_waitcnt vmcnt(0)" ::: "memory");
;             const unsigned og = xb_add(&bar[XB_TOP], 1u);
;             const unsigned tg = og / nx;
;             if (og + 1u == (tg + 1u) * nx) xb_add(&bar[XB_TOPGEN], 1u);
;             else XB_SPIN(xb_ld(&bar[XB_TOPGEN]) == tg, bar);
;             __builtin_amdgcn_fence(__ATOMIC_ACQUIRE, "agent");
;             xb_add(&bar[XB_XGEN(b.x)], 1u);
;             asm volatile("s_waitcnt vmcnt(0)" ::: "memory");
;         } else {
;             XB_SPIN(xb_ld(&bar[XB_XGEN(b.x)]) == gen, bar);
;             __builtin_amdgcn_fence(__ATOMIC_ACQUIRE, "agent");
;             asm volatile("s_waitcnt vmcnt(0)" ::: "memory");
;         }
;     }
;     __syncthreads();
.LBB0_871:
	s_cmp_lt_i32 s95, 6
	s_cbranch_scc1 .LBB0_921
	s_waitcnt vmcnt(0)
	v_cmp_eq_u32_e32 vcc, 0, v0
	s_waitcnt vmcnt(0)
	s_barrier
	s_and_saveexec_b64 s[0:1], vcc
	s_cbranch_execz .LBB0_920
	v_readlane_b32 s4, v246, 22
	v_readlane_b32 s5, v246, 21
	s_waitcnt vmcnt(0) expcnt(0) lgkmcnt(0)
	s_nop 1
	v_mov_b32_e32 v1, s4
	ds_read_b32 v2, v1
	ds_read_b32 v3, v1 offset:4
	ds_read_b32 v4, v1 offset:8
	s_lshl_b32 s5, s5, 6
	s_add_u32 s6, s92, 0xf800
	s_addc_u32 s7, s93, 0
	s_add_u32 s8, s92, 0xfc00
	s_addc_u32 s9, s93, 0
	v_mov_b32_e32 v5, s5
	v_mov_b32_e32 v6, 1
	global_atomic_add v6, v5, v6, s[6:7] sc0
	s_waitcnt lgkmcnt(0)
	v_add_u32_e32 v4, 1, v4
	ds_write_b32 v1, v4 offset:8
	v_mul_lo_u32 v7, v4, v2
	s_waitcnt vmcnt(0)
	v_add_u32_e32 v6, 1, v6
	v_cmp_eq_u32_e32 vcc, v6, v7
	s_and_b64 vcc, exec, vcc
	s_cbranch_vccz .Lgb2_poll
	buffer_wbl2 sc1
	s_waitcnt vmcnt(0)
	s_lshr_b32 s5, s5, 4
	v_mov_b32_e32 v5, s5
	global_atomic_umax v5, v4, s[8:9]

; __device__ __forceinline__ unsigned xb_ld(unsigned* p)              { return __hip_atomic_load(p, __ATOMIC_RELAXED, __HIP_MEMORY_SCOPE_AGENT); }
; __device__ __forceinline__ unsigned xb_add(unsigned* p, unsigned v) { return __hip_atomic_fetch_add(p, v, __ATOMIC_RELAXED, __HIP_MEMORY_SCOPE_AGENT); }
; #define XB_SPIN(cond, bar) do { unsigned _sp = 0; while (cond) { __builtin_amdgcn_s_sleep(1); \
;     if ((++_sp & 255u) == 0u) { if (xb_ld(&(bar)[XB_TMO])) break; if (_sp > XB_SPIN_CAP) { atomicAdd(&(bar)[XB_TMO], 1u); break; } } } } while (0)
; __device__ __forceinline__ void xcd_barrier(const XcdBarrier& b) {
;     asm volatile("s_waitcnt vmcnt(0)" ::: "memory");
;     __syncthreads();
;     if (threadIdx.x == 0) {
;         unsigned* bar = b.bar;
;         __builtin_amdgcn_s_waitcnt(0);
;         unsigned nloc = b.st[0], nx = b.st[1];
;         if (nloc == 0u) { xcd_barrier_complete(bar, b.x, nloc, nx); b.st[0] = nloc; b.st[1] = nx; }
;         const unsigned old = xb_add(&bar[XB_XSUB(b.x)], 1u);
;         const unsigned gen = old / nloc;
;         if (old + 1u == (gen + 1u) * nloc) {
;             __builtin_amdgcn_fence(__ATOMIC_RELEASE, "agent");
;             asm volatile("s_waitcnt vmcnt(0)" ::: "memory");
;             const unsigned og = xb_add(&bar[XB_TOP], 1u);
;             const unsigned tg = og / nx;
;             if (og + 1u == (tg + 1u) * nx) xb_add(&bar[XB_TOPGEN], 1u);
;             else XB_SPIN(xb_ld(&bar[XB_TOPGEN]) == tg, bar);
;             __builtin_amdgcn_fence(__ATOMIC_ACQUIRE, "agent");
;             xb_add(&bar[XB_XGEN(b.x)], 1u);
;             asm volatile("s_waitcnt vmcnt(0)" ::: "memory");
;         } else {
;             XB_SPIN(xb_ld(&bar[XB_XGEN(b.x)]) == gen, bar);
;             __builtin_amdgcn_fence(__ATOMIC_ACQUIRE, "agent");
;             asm volatile("s_waitcnt vmcnt(0)" ::: "memory");
;         }
;     }
;     __syncthreads();
.LBB0_953:
	s_cmp_lt_i32 s95, 7
	s_cbranch_scc1 .LBB0_1003
	s_waitcnt vmcnt(0)
	v_cmp_eq_u32_e32 vcc, 0, v0
	s_waitcnt vmcnt(0) lgkmcnt(0)
	s_barrier
	s_and_saveexec_b64 s[0:1], vcc
	s_cbranch_execz .LBB0_1002
	v_readlane_b32 s4, v246, 22
	v_readlane_b32 s5, v246, 21
	s_waitcnt vmcnt(0) expcnt(0) lgkmcnt(0)
	s_nop 1
	v_mov_b32_e32 v1, s4
	ds_read_b32 v2, v1
	ds_read_b32 v3, v1 offset:4
	ds_read_b32 v4, v1 offset:8
	s_lshl_b32 s5, s5, 6
	s_add_u32 s6, s92, 0xf800
	s_addc_u32 s7, s93, 0
	s_add_u32 s8, s92, 0xfc00
	s_addc_u32 s9, s93, 0
	v_mov_b32_e32 v5, s5
	v_mov_b32_e32 v6, 1
	global_atomic_add v6, v5, v6, s[6:7] sc0
	s_waitcnt lgkmcnt(0)
	v_add_u32_e32 v4, 1, v4
	ds_write_b32 v1, v4 offset:8
	v_mul_lo_u32 v7, v4, v2
	s_waitcnt vmcnt(0)
	v_add_u32_e32 v6, 1, v6
	v_cmp_eq_u32_e32 vcc, v6, v7
	s_and_b64 vcc, exec, vcc
	s_cbranch_vccz .Lgb3_poll
	buffer_wbl2 sc1
	s_waitcnt vmcnt(0)
	s_lshr_b32 s5, s5, 4
	v_mov_b32_e32 v5, s5
	global_atomic_umax v5, v4, s[8:9]

; __device__ __forceinline__ unsigned xb_ld(unsigned* p)              { return __hip_atomic_load(p, __ATOMIC_RELAXED, __HIP_MEMORY_SCOPE_AGENT); }
; __device__ __forceinline__ unsigned xb_add(unsigned* p, unsigned v) { return __hip_atomic_fetch_add(p, v, __ATOMIC_RELAXED, __HIP_MEMORY_SCOPE_AGENT); }
; #define XB_SPIN(cond, bar) do { unsigned _sp = 0; while (cond) { __builtin_amdgcn_s_sleep(1); \
;     if ((++_sp & 255u) == 0u) { if (xb_ld(&(bar)[XB_TMO])) break; if (_sp > XB_SPIN_CAP) { atomicAdd(&(bar)[XB_TMO], 1u); break; } } } } while (0)
; __device__ __forceinline__ void xcd_barrier(const XcdBarrier& b) {
;     asm volatile("s_waitcnt vmcnt(0)" ::: "memory");
;     __syncthreads();
;     if (threadIdx.x == 0) {
;         unsigned* bar = b.bar;
;         __builtin_amdgcn_s_waitcnt(0);
;         unsigned nloc = b.st[0], nx = b.st[1];
;         if (nloc == 0u) { xcd_barrier_complete(bar, b.x, nloc, nx); b.st[0] = nloc; b.st[1] = nx; }
;         const unsigned old = xb_add(&bar[XB_XSUB(b.x)], 1u);
;         const unsigned gen = old / nloc;
;         if (old + 1u == (gen + 1u) * nloc) {
;             __builtin_amdgcn_fence(__ATOMIC_RELEASE, "agent");
;             asm volatile("s_waitcnt vmcnt(0)" ::: "memory");
;             const unsigned og = xb_add(&bar[XB_TOP], 1u);
;             const unsigned tg = og / nx;
;             if (og + 1u == (tg + 1u) * nx) xb_add(&bar[XB_TOPGEN], 1u);
;             else XB_SPIN(xb_ld(&bar[XB_TOPGEN]) == tg, bar);
;             __builtin_amdgcn_fence(__ATOMIC_ACQUIRE, "agent");
;             xb_add(&bar[XB_XGEN(b.x)], 1u);
;             asm volatile("s_waitcnt vmcnt(0)" ::: "memory");
;         } else {
;             XB_SPIN(xb_ld(&bar[XB_XGEN(b.x)]) == gen, bar);
;             __builtin_amdgcn_fence(__ATOMIC_ACQUIRE, "agent");
;             asm volatile("s_waitcnt vmcnt(0)" ::: "memory");
;         }
;     }
;     __syncthreads();
.LBB0_1030:
	s_cmp_lt_i32 s95, 8
	s_cbranch_scc1 .LBB0_1080
	s_waitcnt vmcnt(0)
	v_cmp_eq_u32_e32 vcc, 0, v0
	s_waitcnt vmcnt(0) lgkmcnt(0)
	s_barrier
	s_and_saveexec_b64 s[0:1], vcc
	s_cbranch_execz .LBB0_1079
	v_readlane_b32 s4, v246, 22
	v_readlane_b32 s5, v246, 21
	s_waitcnt vmcnt(0) expcnt(0) lgkmcnt(0)
	s_nop 1
	v_mov_b32_e32 v1, s4
	ds_read_b32 v2, v1
	ds_read_b32 v3, v1 offset:4
	ds_read_b32 v4, v1 offset:8
	s_lshl_b32 s5, s5, 6
	s_add_u32 s6, s92, 0xf800
	s_addc_u32 s7, s93, 0
	s_add_u32 s8, s92, 0xfc00
	s_addc_u32 s9, s93, 0
	v_mov_b32_e32 v5, s5
	v_mov_b32_e32 v6, 1
	global_atomic_add v6, v5, v6, s[6:7] sc0
	s_waitcnt lgkmcnt(0)
	v_add_u32_e32 v4, 1, v4
	ds_write_b32 v1, v4 offset:8
	v_mul_lo_u32 v7, v4, v2
	s_waitcnt vmcnt(0)
	v_add_u32_e32 v6, 1, v6
	v_cmp_eq_u32_e32 vcc, v6, v7
	s_and_b64 vcc, exec, vcc
	s_cbranch_vccz .Lgb4_poll
	buffer_wbl2 sc1
	s_waitcnt vmcnt(0)
	s_lshr_b32 s5, s5, 4
	v_mov_b32_e32 v5, s5
	global_atomic_umax v5, v4, s[8:9]

; __device__ __forceinline__ unsigned xb_ld(unsigned* p)              { return __hip_atomic_load(p, __ATOMIC_RELAXED, __HIP_MEMORY_SCOPE_AGENT); }
; __device__ __forceinline__ unsigned xb_add(unsigned* p, unsigned v) { return __hip_atomic_fetch_add(p, v, __ATOMIC_RELAXED, __HIP_MEMORY_SCOPE_AGENT); }
; #define XB_SPIN(cond, bar) do { unsigned _sp = 0; while (cond) { __builtin_amdgcn_s_sleep(1); \
;     if ((++_sp & 255u) == 0u) { if (xb_ld(&(bar)[XB_TMO])) break; if (_sp > XB_SPIN_CAP) { atomicAdd(&(bar)[XB_TMO], 1u); break; } } } } while (0)
; __device__ __forceinline__ void xcd_barrier(const XcdBarrier& b) {
;     asm volatile("s_waitcnt vmcnt(0)" ::: "memory");
;     __syncthreads();
;     if (threadIdx.x == 0) {
;         unsigned* bar = b.bar;
;         __builtin_amdgcn_s_waitcnt(0);
;         unsigned nloc = b.st[0], nx = b.st[1];
;         if (nloc == 0u) { xcd_barrier_complete(bar, b.x, nloc, nx); b.st[0] = nloc; b.st[1] = nx; }
;         const unsigned old = xb_add(&bar[XB_XSUB(b.x)], 1u);
;         const unsigned gen = old / nloc;
;         if (old + 1u == (gen + 1u) * nloc) {
;             __builtin_amdgcn_fence(__ATOMIC_RELEASE, "agent");
;             asm volatile("s_waitcnt vmcnt(0)" ::: "memory");
;             const unsigned og = xb_add(&bar[XB_TOP], 1u);
;             const unsigned tg = og / nx;
;             if (og + 1u == (tg + 1u) * nx) xb_add(&bar[XB_TOPGEN], 1u);
;             else XB_SPIN(xb_ld(&bar[XB_TOPGEN]) == tg, bar);
;             __builtin_amdgcn_fence(__ATOMIC_ACQUIRE, "agent");
;             xb_add(&bar[XB_XGEN(b.x)], 1u);
;             asm volatile("s_waitcnt vmcnt(0)" ::: "memory");
;         } else {
;             XB_SPIN(xb_ld(&bar[XB_XGEN(b.x)]) == gen, bar);
;             __builtin_amdgcn_fence(__ATOMIC_ACQUIRE, "agent");
;             asm volatile("s_waitcnt vmcnt(0)" ::: "memory");
;         }
;     }
;     __syncthreads();
.LBB0_1102:
	s_cmp_lt_i32 s95, 9
	s_cbranch_scc1 .LBB0_1152
	s_waitcnt vmcnt(0)
	v_cmp_eq_u32_e32 vcc, 0, v0
	s_waitcnt vmcnt(0) lgkmcnt(0)
	s_barrier
	s_and_saveexec_b64 s[0:1], vcc
	s_cbranch_execz .LBB0_1151
	v_readlane_b32 s4, v246, 22
	v_readlane_b32 s5, v246, 21
	s_waitcnt vmcnt(0) expcnt(0) lgkmcnt(0)
	s_nop 1
	v_mov_b32_e32 v1, s4
	ds_read_b32 v2, v1
	ds_read_b32 v3, v1 offset:4
	ds_read_b32 v4, v1 offset:8
	s_lshl_b32 s5, s5, 6
	s_add_u32 s6, s92, 0xf800
	s_addc_u32 s7, s93, 0
	s_add_u32 s8, s92, 0xfc00
	s_addc_u32 s9, s93, 0
	v_mov_b32_e32 v5, s5
	v_mov_b32_e32 v6, 1
	global_atomic_add v6, v5, v6, s[6:7] sc0
	s_waitcnt lgkmcnt(0)
	v_add_u32_e32 v4, 1, v4
	ds_write_b32 v1, v4 offset:8
	v_mul_lo_u32 v7, v4, v2
	s_waitcnt vmcnt(0)
	v_add_u32_e32 v6, 1, v6
	v_cmp_eq_u32_e32 vcc, v6, v7
	s_and_b64 vcc, exec, vcc
	s_cbranch_vccz .Lgb5_poll
	buffer_wbl2 sc1
	s_waitcnt vmcnt(0)
	s_lshr_b32 s5, s5, 4
	v_mov_b32_e32 v5, s5
	global_atomic_umax v5, v4, s[8:9]

; __device__ __forceinline__ unsigned xb_ld(unsigned* p)              { return __hip_atomic_load(p, __ATOMIC_RELAXED, __HIP_MEMORY_SCOPE_AGENT); }
; __device__ __forceinline__ unsigned xb_add(unsigned* p, unsigned v) { return __hip_atomic_fetch_add(p, v, __ATOMIC_RELAXED, __HIP_MEMORY_SCOPE_AGENT); }
; #define XB_SPIN(cond, bar) do { unsigned _sp = 0; while (cond) { __builtin_amdgcn_s_sleep(1); \
;     if ((++_sp & 255u) == 0u) { if (xb_ld(&(bar)[XB_TMO])) break; if (_sp > XB_SPIN_CAP) { atomicAdd(&(bar)[XB_TMO], 1u); break; } } } } while (0)
; __device__ __forceinline__ void xcd_barrier(const XcdBarrier& b) {
;     asm volatile("s_waitcnt vmcnt(0)" ::: "memory");
;     __syncthreads();
;     if (threadIdx.x == 0) {
;         unsigned* bar = b.bar;
;         __builtin_amdgcn_s_waitcnt(0);
;         unsigned nloc = b.st[0], nx = b.st[1];
;         if (nloc == 0u) { xcd_barrier_complete(bar, b.x, nloc, nx); b.st[0] = nloc; b.st[1] = nx; }
;         const unsigned old = xb_add(&bar[XB_XSUB(b.x)], 1u);
;         const unsigned gen = old / nloc;
;         if (old + 1u == (gen + 1u) * nloc) {
;             __builtin_amdgcn_fence(__ATOMIC_RELEASE, "agent");
;             asm volatile("s_waitcnt vmcnt(0)" ::: "memory");
;             const unsigned og = xb_add(&bar[XB_TOP], 1u);
;             const unsigned tg = og / nx;
;             if (og + 1u == (tg + 1u) * nx) xb_add(&bar[XB_TOPGEN], 1u);
;             else XB_SPIN(xb_ld(&bar[XB_TOPGEN]) == tg, bar);
;             __builtin_amdgcn_fence(__ATOMIC_ACQUIRE, "agent");
;             xb_add(&bar[XB_XGEN(b.x)], 1u);
;             asm volatile("s_waitcnt vmcnt(0)" ::: "memory");
;         } else {
;             XB_SPIN(xb_ld(&bar[XB_XGEN(b.x)]) == gen, bar);
;             __builtin_amdgcn_fence(__ATOMIC_ACQUIRE, "agent");
;             asm volatile("s_waitcnt vmcnt(0)" ::: "memory");
;         }
;     }
;     __syncthreads();
.LBB0_1228:
	s_cmp_lt_i32 s95, 10
	v_readlane_b32 s97, v246, 24
	s_cbranch_scc1 .LBB0_1278
	s_waitcnt vmcnt(0)
	v_cmp_eq_u32_e32 vcc, 0, v0
	s_waitcnt vmcnt(0) lgkmcnt(0)
	s_barrier
	s_and_saveexec_b64 s[0:1], vcc
	v_readlane_b32 s46, v246, 22
	s_cbranch_execz .LBB0_1277
	v_readlane_b32 s4, v246, 22
	v_readlane_b32 s5, v246, 21
	s_waitcnt vmcnt(0) expcnt(0) lgkmcnt(0)
	s_nop 1
	v_mov_b32_e32 v1, s4
	ds_read_b32 v2, v1
	ds_read_b32 v3, v1 offset:4
	ds_read_b32 v4, v1 offset:8
	s_lshl_b32 s5, s5, 6
	s_add_u32 s6, s92, 0xf800
	s_addc_u32 s7, s93, 0
	s_add_u32 s8, s92, 0xfc00
	s_addc_u32 s9, s93, 0
	v_mov_b32_e32 v5, s5
	v_mov_b32_e32 v6, 1
	global_atomic_add v6, v5, v6, s[6:7] sc0
	s_waitcnt lgkmcnt(0)
	v_add_u32_e32 v4, 1, v4
	ds_write_b32 v1, v4 offset:8
	v_mul_lo_u32 v7, v4, v2
	s_waitcnt vmcnt(0)
	v_add_u32_e32 v6, 1, v6
	v_cmp_eq_u32_e32 vcc, v6, v7
	s_and_b64 vcc, exec, vcc
	s_cbranch_vccz .Lgb6_poll
	buffer_wbl2 sc1
	s_waitcnt vmcnt(0)
	s_lshr_b32 s5, s5, 4
	v_mov_b32_e32 v5, s5
	global_atomic_umax v5, v4, s[8:9]

; __device__ __forceinline__ unsigned xb_ld(unsigned* p)              { return __hip_atomic_load(p, __ATOMIC_RELAXED, __HIP_MEMORY_SCOPE_AGENT); }
; __device__ __forceinline__ unsigned xb_add(unsigned* p, unsigned v) { return __hip_atomic_fetch_add(p, v, __ATOMIC_RELAXED, __HIP_MEMORY_SCOPE_AGENT); }
; #define XB_SPIN(cond, bar) do { unsigned _sp = 0; while (cond) { __builtin_amdgcn_s_sleep(1); \
;     if ((++_sp & 255u) == 0u) { if (xb_ld(&(bar)[XB_TMO])) break; if (_sp > XB_SPIN_CAP) { atomicAdd(&(bar)[XB_TMO], 1u); break; } } } } while (0)
; __device__ __forceinline__ void xcd_barrier(const XcdBarrier& b) {
;     asm volatile("s_waitcnt vmcnt(0)" ::: "memory");
;     __syncthreads();
;     if (threadIdx.x == 0) {
;         unsigned* bar = b.bar;
;         __builtin_amdgcn_s_waitcnt(0);
;         unsigned nloc = b.st[0], nx = b.st[1];
;         if (nloc == 0u) { xcd_barrier_complete(bar, b.x, nloc, nx); b.st[0] = nloc; b.st[1] = nx; }
;         const unsigned old = xb_add(&bar[XB_XSUB(b.x)], 1u);
;         const unsigned gen = old / nloc;
;         if (old + 1u == (gen + 1u) * nloc) {
;             __builtin_amdgcn_fence(__ATOMIC_RELEASE, "agent");
;             asm volatile("s_waitcnt vmcnt(0)" ::: "memory");
;             const unsigned og = xb_add(&bar[XB_TOP], 1u);
;             const unsigned tg = og / nx;
;             if (og + 1u == (tg + 1u) * nx) xb_add(&bar[XB_TOPGEN], 1u);
;             else XB_SPIN(xb_ld(&bar[XB_TOPGEN]) == tg, bar);
;             __builtin_amdgcn_fence(__ATOMIC_ACQUIRE, "agent");
;             xb_add(&bar[XB_XGEN(b.x)], 1u);
;             asm volatile("s_waitcnt vmcnt(0)" ::: "memory");
;         } else {
;             XB_SPIN(xb_ld(&bar[XB_XGEN(b.x)]) == gen, bar);
;             __builtin_amdgcn_fence(__ATOMIC_ACQUIRE, "agent");
;             asm volatile("s_waitcnt vmcnt(0)" ::: "memory");
;         }
;     }
;     __syncthreads();
.LBB0_1321:
	s_cmp_lt_i32 s95, 11
	s_cbranch_scc1 .LBB0_1371
	s_waitcnt vmcnt(0)
	v_cmp_eq_u32_e32 vcc, 0, v0
	s_waitcnt vmcnt(0) lgkmcnt(0)
	s_barrier
	s_and_saveexec_b64 s[0:1], vcc
	s_cbranch_execz .LBB0_1370
	v_readlane_b32 s4, v246, 22
	v_readlane_b32 s5, v246, 21
	s_waitcnt vmcnt(0) expcnt(0) lgkmcnt(0)
	s_nop 1
	v_mov_b32_e32 v1, s4
	ds_read_b32 v2, v1
	ds_read_b32 v3, v1 offset:4
	ds_read_b32 v4, v1 offset:8
	s_lshl_b32 s5, s5, 6
	s_add_u32 s6, s92, 0xf800
	s_addc_u32 s7, s93, 0
	s_add_u32 s8, s92, 0xfc00
	s_addc_u32 s9, s93, 0
	v_mov_b32_e32 v5, s5
	v_mov_b32_e32 v6, 1
	global_atomic_add v6, v5, v6, s[6:7] sc0
	s_waitcnt lgkmcnt(0)
	v_add_u32_e32 v4, 1, v4
	ds_write_b32 v1, v4 offset:8
	v_mul_lo_u32 v7, v4, v2
	s_waitcnt vmcnt(0)
	v_add_u32_e32 v6, 1, v6
	v_cmp_eq_u32_e32 vcc, v6, v7
	s_and_b64 vcc, exec, vcc
	s_cbranch_vccz .Lgb7_poll
	buffer_wbl2 sc1
	s_waitcnt vmcnt(0)
	s_lshr_b32 s5, s5, 4
	v_mov_b32_e32 v5, s5
	global_atomic_umax v5, v4, s[8:9]

; __device__ __forceinline__ unsigned xb_ld(unsigned* p)              { return __hip_atomic_load(p, __ATOMIC_RELAXED, __HIP_MEMORY_SCOPE_AGENT); }
; __device__ __forceinline__ unsigned xb_add(unsigned* p, unsigned v) { return __hip_atomic_fetch_add(p, v, __ATOMIC_RELAXED, __HIP_MEMORY_SCOPE_AGENT); }
; #define XB_SPIN(cond, bar) do { unsigned _sp = 0; while (cond) { __builtin_amdgcn_s_sleep(1); \
;     if ((++_sp & 255u) == 0u) { if (xb_ld(&(bar)[XB_TMO])) break; if (_sp > XB_SPIN_CAP) { atomicAdd(&(bar)[XB_TMO], 1u); break; } } } } while (0)
; __device__ __forceinline__ void xcd_barrier(const XcdBarrier& b) {
;     asm volatile("s_waitcnt vmcnt(0)" ::: "memory");
;     __syncthreads();
;     if (threadIdx.x == 0) {
;         unsigned* bar = b.bar;
;         __builtin_amdgcn_s_waitcnt(0);
;         unsigned nloc = b.st[0], nx = b.st[1];
;         if (nloc == 0u) { xcd_barrier_complete(bar, b.x, nloc, nx); b.st[0] = nloc; b.st[1] = nx; }
;         const unsigned old = xb_add(&bar[XB_XSUB(b.x)], 1u);
;         const unsigned gen = old / nloc;
;         if (old + 1u == (gen + 1u) * nloc) {
;             __builtin_amdgcn_fence(__ATOMIC_RELEASE, "agent");
;             asm volatile("s_waitcnt vmcnt(0)" ::: "memory");
;             const unsigned og = xb_add(&bar[XB_TOP], 1u);
;             const unsigned tg = og / nx;
;             if (og + 1u == (tg + 1u) * nx) xb_add(&bar[XB_TOPGEN], 1u);
;             else XB_SPIN(xb_ld(&bar[XB_TOPGEN]) == tg, bar);
;             __builtin_amdgcn_fence(__ATOMIC_ACQUIRE, "agent");
;             xb_add(&bar[XB_XGEN(b.x)], 1u);
;             asm volatile("s_waitcnt vmcnt(0)" ::: "memory");
;         } else {
;             XB_SPIN(xb_ld(&bar[XB_XGEN(b.x)]) == gen, bar);
;             __builtin_amdgcn_fence(__ATOMIC_ACQUIRE, "agent");
;             asm volatile("s_waitcnt vmcnt(0)" ::: "memory");
;         }
;     }
;     __syncthreads();
.LBB0_1412:
	s_cmp_lt_i32 s95, 12
	s_cbranch_scc1 .LBB0_1462
	s_waitcnt vmcnt(0)
	v_cmp_eq_u32_e32 vcc, 0, v0
	s_waitcnt vmcnt(0) lgkmcnt(0)
	s_barrier
	s_and_saveexec_b64 s[0:1], vcc
	s_cbranch_execz .LBB0_1461
	v_readlane_b32 s4, v246, 22
	v_readlane_b32 s5, v246, 21
	s_waitcnt vmcnt(0) expcnt(0) lgkmcnt(0)
	s_nop 1
	v_mov_b32_e32 v1, s4
	ds_read_b32 v2, v1
	ds_read_b32 v3, v1 offset:4
	ds_read_b32 v4, v1 offset:8
	s_lshl_b32 s5, s5, 6
	s_add_u32 s6, s92, 0xf800
	s_addc_u32 s7, s93, 0
	s_add_u32 s8, s92, 0xfc00
	s_addc_u32 s9, s93, 0
	v_mov_b32_e32 v5, s5
	v_mov_b32_e32 v6, 1
	global_atomic_add v6, v5, v6, s[6:7] sc0
	s_waitcnt lgkmcnt(0)
	v_add_u32_e32 v4, 1, v4
	ds_write_b32 v1, v4 offset:8
	v_mul_lo_u32 v7, v4, v2
	s_waitcnt vmcnt(0)
	v_add_u32_e32 v6, 1, v6
	v_cmp_eq_u32_e32 vcc, v6, v7
	s_and_b64 vcc, exec, vcc
	s_cbranch_vccz .Lgb8_poll
	buffer_wbl2 sc1
	s_waitcnt vmcnt(0)
	s_lshr_b32 s5, s5, 4
	v_mov_b32_e32 v5, s5
	global_atomic_umax v5, v4, s[8:9]
